# k_agg1: gather addresses via v_mad_u32_u16 with op_sel (index*128+lane offset in one VALU op instead of sdwa shift + or)
# speedup vs baseline: 1.0072x; 1.0050x over previous
_Z6k_agg1PKDF16_PK15HIP_vector_typeIiLj2EEPKtPKfS8_S8_Pf:
	s_and_b32 s8, s2, 3
	s_lshl_b32 s3, s8, 6
	s_movk_i32 s34, 0x80
	v_add_u32_e32 v6, 0x140, v0
	s_load_dwordx4 s[4:7], s[0:1], 0x20
	s_load_dwordx2 s[28:29], s[0:1], 0x30
	v_and_b32_e32 v1, 7, v0
	v_and_or_b32 v4, v0, 56, s3
	v_lshrrev_b32_e32 v2, 6, v0
	v_lshrrev_b32_e32 v10, 6, v6
	v_cmp_eq_u32_e64 s[18:19], 7, v1
	v_or_b32_e32 v5, v2, v4
	v_and_or_b32 v4, v10, 7, v4
	v_cndmask_b32_e64 v3, v1, 0, s[18:19]
	v_mul_u32_u24_e32 v5, 7, v5
	v_mul_u32_u24_e32 v4, 7, v4
	v_add_lshl_u32 v5, v5, v3, 2
	v_add_lshl_u32 v3, v4, v3, 2
	s_waitcnt lgkmcnt(0)
	global_load_dword v12, v5, s[6:7]
	global_load_dword v13, v3, s[6:7]
	v_and_b32_e32 v3, 63, v0
	v_or_b32_e32 v3, s3, v3
	v_lshlrev_b32_e32 v3, 2, v3
	global_load_dword v20, v3, s[4:5]
	s_load_dwordx8 s[20:27], s[0:1], 0x0
	s_lshr_b32 s6, s2, 2
	v_lshlrev_b32_e32 v3, 2, v0
	s_movk_i32 s30, 0xe0
	s_movk_i32 s3, 0x200
	s_movk_i32 s4, 0xc0
	s_mul_i32 s31, s8, 0x61a880
	v_mad_u64_u32 v[8:9], s[6:7], s6, 5, v[2:3]
	v_lshlrev_b32_e32 v4, 2, v1
	v_mov_b32_e32 v5, 0
	v_bfe_u32 v21, v0, 3, 3
	v_cmp_gt_u32_e32 vcc, 64, v0
	v_cmp_gt_u32_e64 s[0:1], s3, v0
	v_cmp_gt_u32_e64 s[2:3], s4, v0
	v_cmp_ne_u32_e64 s[4:5], 7, v1
	v_lshlrev_b32_e32 v6, 4, v1
	v_lshlrev_b32_e32 v22, 5, v1
	v_mul_u32_u24_e32 v0, 28, v1
	v_cmp_eq_u32_e64 s[6:7], 1, v1
	v_cmp_eq_u32_e64 s[8:9], 2, v1
	v_cmp_eq_u32_e64 s[10:11], 3, v1
	v_cmp_eq_u32_e64 s[12:13], 4, v1
	v_cmp_eq_u32_e64 s[14:15], 5, v1
	v_cmp_eq_u32_e64 s[16:17], 6, v1
	v_and_or_b32 v1, v3, s30, v4
	s_waitcnt lgkmcnt(0)
	s_add_u32 s20, s20, s31
	s_mov_b32 s33, 0
	v_or_b32_e32 v9, 0x800, v3
	v_mov_b32_e32 v7, v6
	v_add_u32_e32 v23, v4, v0
	v_lshl_or_b32 v24, v2, 8, v1
	v_lshl_or_b32 v25, v10, 8, v1
	v_lshl_add_u64 v[10:11], s[28:29], 0, v[4:5]
	s_addc_u32 s21, s21, 0
	v_mov_b32_e32 v28, 7
	s_waitcnt vmcnt(2)
	v_cndmask_b32_e64 v26, v12, 0, s[18:19]
	s_waitcnt vmcnt(1)
	v_cndmask_b32_e64 v27, v13, 0, s[18:19]
	s_branch .LBB3_2

.Lagg_full:
	global_load_dwordx4 v[30:33], v[2:3], off
	v_add_u32_e32 v0, 8, v0
	v_cmp_ge_i32_e64 s[18:19], v0, v1
	v_lshl_add_u64 v[2:3], v[2:3], 0, 16
	s_or_b64 s[30:31], s[18:19], s[30:31]
	s_waitcnt vmcnt(0)
	v_mad_u32_u16 v39, v30, s34, v6
	v_mad_u32_u16 v38, v30, s34, v6 op_sel:[1,0,0,0]
	v_mad_u32_u16 v40, v31, s34, v6
	v_mad_u32_u16 v42, v31, s34, v6 op_sel:[1,0,0,0]
	v_mad_u32_u16 v46, v32, s34, v6
	v_mad_u32_u16 v50, v32, s34, v6 op_sel:[1,0,0,0]
	v_mad_u32_u16 v54, v33, s34, v6
	v_mad_u32_u16 v58, v33, s34, v6 op_sel:[1,0,0,0]
	global_load_dwordx4 v[30:33], v39, s[20:21]
	global_load_dwordx4 v[34:37], v38, s[20:21]
	s_nop 0
	global_load_dwordx4 v[38:41], v40, s[20:21]
	s_nop 0
	global_load_dwordx4 v[42:45], v42, s[20:21]
	s_nop 0
	global_load_dwordx4 v[46:49], v46, s[20:21]
	s_nop 0
	global_load_dwordx4 v[50:53], v50, s[20:21]
	s_nop 0
	global_load_dwordx4 v[54:57], v54, s[20:21]
	s_nop 0
	global_load_dwordx4 v[58:61], v58, s[20:21]
	s_waitcnt vmcnt(6)
	v_pk_add_f16 v33, v33, v37
	v_pk_add_f16 v32, v32, v36
	v_pk_add_f16 v31, v31, v35
	v_pk_add_f16 v30, v30, v34
	s_waitcnt vmcnt(4)
	v_pk_add_f16 v34, v41, v45
	v_pk_add_f16 v35, v40, v44
	v_pk_add_f16 v36, v39, v43
	v_pk_add_f16 v37, v38, v42
	s_waitcnt vmcnt(2)
	v_pk_add_f16 v38, v49, v53
	v_pk_add_f16 v39, v48, v52
	v_pk_add_f16 v40, v47, v51
	v_pk_add_f16 v41, v46, v50
	s_waitcnt vmcnt(0)
	v_pk_add_f16 v42, v57, v61
	v_pk_add_f16 v43, v56, v60
	v_pk_add_f16 v44, v55, v59
	v_pk_add_f16 v45, v54, v58
	v_pk_add_f16 v30, v30, v37
	v_pk_add_f16 v31, v31, v36
	v_pk_add_f16 v32, v32, v35
	v_pk_add_f16 v33, v33, v34
	v_pk_add_f16 v34, v41, v45
	v_pk_add_f16 v35, v40, v44
	v_pk_add_f16 v36, v39, v43
	v_pk_add_f16 v37, v38, v42
	v_pk_add_f16 v36, v32, v36
	v_pk_add_f16 v37, v33, v37
	v_pk_add_f16 v33, v31, v35
	v_pk_add_f16 v31, v30, v34
	v_cvt_f32_f16_e32 v32, v33
	v_cvt_f32_f16_e32 v30, v31
	v_cvt_f32_f16_sdwa v31, v31 dst_sel:DWORD dst_unused:UNUSED_PAD src0_sel:WORD_1
	v_cvt_f32_f16_sdwa v33, v33 dst_sel:DWORD dst_unused:UNUSED_PAD src0_sel:WORD_1
	v_cvt_f32_f16_e32 v34, v36
	v_cvt_f32_f16_sdwa v35, v36 dst_sel:DWORD dst_unused:UNUSED_PAD src0_sel:WORD_1
	v_cvt_f32_f16_e32 v36, v37
	v_cvt_f32_f16_sdwa v37, v37 dst_sel:DWORD dst_unused:UNUSED_PAD src0_sel:WORD_1
	v_pk_add_f32 v[18:19], v[18:19], v[30:31]
	v_pk_add_f32 v[16:17], v[16:17], v[32:33]
	v_pk_add_f32 v[14:15], v[14:15], v[34:35]
	v_pk_add_f32 v[12:13], v[12:13], v[36:37]
	s_andn2_b64 exec, exec, s[30:31]
	s_cbranch_execnz .LBB3_4
	s_branch .Lagg_loop_done
.Lagg_n1:
	global_load_dword v30, v[2:3], off
	s_waitcnt vmcnt(0)
	v_mad_u32_u16 v39, v30, s34, v6
	global_load_dwordx4 v[30:33], v39, s[20:21]
	s_nop 0
	s_waitcnt vmcnt(0)
	v_cvt_f32_f16_e32 v34, v30
	v_cvt_f32_f16_sdwa v35, v30 dst_sel:DWORD dst_unused:UNUSED_PAD src0_sel:WORD_1
	v_cvt_f32_f16_e32 v36, v31
	v_cvt_f32_f16_sdwa v37, v31 dst_sel:DWORD dst_unused:UNUSED_PAD src0_sel:WORD_1
	v_cvt_f32_f16_e32 v38, v32
	v_cvt_f32_f16_sdwa v39, v32 dst_sel:DWORD dst_unused:UNUSED_PAD src0_sel:WORD_1
	v_cvt_f32_f16_e32 v40, v33
	v_cvt_f32_f16_sdwa v41, v33 dst_sel:DWORD dst_unused:UNUSED_PAD src0_sel:WORD_1
	v_pk_add_f32 v[18:19], v[18:19], v[34:35]
	v_pk_add_f32 v[16:17], v[16:17], v[36:37]
	v_pk_add_f32 v[14:15], v[14:15], v[38:39]
	v_pk_add_f32 v[12:13], v[12:13], v[40:41]
	s_branch .Lagg_loop_done
.Lagg_n2:
	global_load_dword v30, v[2:3], off
	s_waitcnt vmcnt(0)
	v_mad_u32_u16 v39, v30, s34, v6
	v_mad_u32_u16 v38, v30, s34, v6 op_sel:[1,0,0,0]
	global_load_dwordx4 v[30:33], v39, s[20:21]
	s_nop 0
	global_load_dwordx4 v[34:37], v38, s[20:21]
	s_nop 0
	s_waitcnt vmcnt(0)
	v_pk_add_f16 v33, v33, v37
	v_pk_add_f16 v32, v32, v36
	v_pk_add_f16 v31, v31, v35
	v_pk_add_f16 v30, v30, v34
	v_cvt_f32_f16_e32 v34, v30
	v_cvt_f32_f16_sdwa v35, v30 dst_sel:DWORD dst_unused:UNUSED_PAD src0_sel:WORD_1
	v_cvt_f32_f16_e32 v36, v31
	v_cvt_f32_f16_sdwa v37, v31 dst_sel:DWORD dst_unused:UNUSED_PAD src0_sel:WORD_1
	v_cvt_f32_f16_e32 v38, v32
	v_cvt_f32_f16_sdwa v39, v32 dst_sel:DWORD dst_unused:UNUSED_PAD src0_sel:WORD_1
	v_cvt_f32_f16_e32 v40, v33
	v_cvt_f32_f16_sdwa v41, v33 dst_sel:DWORD dst_unused:UNUSED_PAD src0_sel:WORD_1
	v_pk_add_f32 v[18:19], v[18:19], v[34:35]
	v_pk_add_f32 v[16:17], v[16:17], v[36:37]
	v_pk_add_f32 v[14:15], v[14:15], v[38:39]
	v_pk_add_f32 v[12:13], v[12:13], v[40:41]
	s_branch .Lagg_loop_done
.Lagg_n3:
	global_load_dwordx2 v[30:31], v[2:3], off
	s_waitcnt vmcnt(0)
	v_mad_u32_u16 v39, v30, s34, v6
	v_mad_u32_u16 v38, v30, s34, v6 op_sel:[1,0,0,0]
	v_mad_u32_u16 v40, v31, s34, v6
	global_load_dwordx4 v[30:33], v39, s[20:21]
	s_nop 0
	global_load_dwordx4 v[34:37], v38, s[20:21]
	s_nop 0
	global_load_dwordx4 v[38:41], v40, s[20:21]
	s_nop 0
	s_waitcnt vmcnt(1)
	v_pk_add_f16 v33, v33, v37
	v_pk_add_f16 v32, v32, v36
	v_pk_add_f16 v31, v31, v35
	v_pk_add_f16 v30, v30, v34
	s_waitcnt vmcnt(0)
	v_pk_add_f16 v30, v30, v38
	v_pk_add_f16 v31, v31, v39
	v_pk_add_f16 v32, v32, v40
	v_pk_add_f16 v33, v33, v41
	v_cvt_f32_f16_e32 v34, v30
	v_cvt_f32_f16_sdwa v35, v30 dst_sel:DWORD dst_unused:UNUSED_PAD src0_sel:WORD_1
	v_cvt_f32_f16_e32 v36, v31
	v_cvt_f32_f16_sdwa v37, v31 dst_sel:DWORD dst_unused:UNUSED_PAD src0_sel:WORD_1
	v_cvt_f32_f16_e32 v38, v32
	v_cvt_f32_f16_sdwa v39, v32 dst_sel:DWORD dst_unused:UNUSED_PAD src0_sel:WORD_1
	v_cvt_f32_f16_e32 v40, v33
	v_cvt_f32_f16_sdwa v41, v33 dst_sel:DWORD dst_unused:UNUSED_PAD src0_sel:WORD_1
	v_pk_add_f32 v[18:19], v[18:19], v[34:35]
	v_pk_add_f32 v[16:17], v[16:17], v[36:37]
	v_pk_add_f32 v[14:15], v[14:15], v[38:39]
	v_pk_add_f32 v[12:13], v[12:13], v[40:41]
	s_branch .Lagg_loop_done
.Lagg_n4:
	global_load_dwordx2 v[30:31], v[2:3], off
	s_waitcnt vmcnt(0)
	v_mad_u32_u16 v39, v30, s34, v6
	v_mad_u32_u16 v38, v30, s34, v6 op_sel:[1,0,0,0]
	v_mad_u32_u16 v40, v31, s34, v6
	v_mad_u32_u16 v42, v31, s34, v6 op_sel:[1,0,0,0]
	global_load_dwordx4 v[30:33], v39, s[20:21]
	s_nop 0
	global_load_dwordx4 v[34:37], v38, s[20:21]
	s_nop 0
	global_load_dwordx4 v[38:41], v40, s[20:21]
	s_nop 0
	global_load_dwordx4 v[42:45], v42, s[20:21]
	s_nop 0
	s_waitcnt vmcnt(2)
	v_pk_add_f16 v33, v33, v37
	v_pk_add_f16 v32, v32, v36
	v_pk_add_f16 v31, v31, v35
	v_pk_add_f16 v30, v30, v34
	s_waitcnt vmcnt(0)
	v_pk_add_f16 v34, v41, v45
	v_pk_add_f16 v35, v40, v44
	v_pk_add_f16 v36, v39, v43
	v_pk_add_f16 v37, v38, v42
	v_pk_add_f16 v30, v30, v37
	v_pk_add_f16 v31, v31, v36
	v_pk_add_f16 v32, v32, v35
	v_pk_add_f16 v33, v33, v34
	v_cvt_f32_f16_e32 v34, v30
	v_cvt_f32_f16_sdwa v35, v30 dst_sel:DWORD dst_unused:UNUSED_PAD src0_sel:WORD_1
	v_cvt_f32_f16_e32 v36, v31
	v_cvt_f32_f16_sdwa v37, v31 dst_sel:DWORD dst_unused:UNUSED_PAD src0_sel:WORD_1
	v_cvt_f32_f16_e32 v38, v32
	v_cvt_f32_f16_sdwa v39, v32 dst_sel:DWORD dst_unused:UNUSED_PAD src0_sel:WORD_1
	v_cvt_f32_f16_e32 v40, v33
	v_cvt_f32_f16_sdwa v41, v33 dst_sel:DWORD dst_unused:UNUSED_PAD src0_sel:WORD_1
	v_pk_add_f32 v[18:19], v[18:19], v[34:35]
	v_pk_add_f32 v[16:17], v[16:17], v[36:37]
	v_pk_add_f32 v[14:15], v[14:15], v[38:39]
	v_pk_add_f32 v[12:13], v[12:13], v[40:41]
	s_branch .Lagg_loop_done
.Lagg_n5:
	global_load_dwordx3 v[30:32], v[2:3], off
	s_waitcnt vmcnt(0)
	v_mad_u32_u16 v39, v30, s34, v6
	v_mad_u32_u16 v38, v30, s34, v6 op_sel:[1,0,0,0]
	v_mad_u32_u16 v40, v31, s34, v6
	v_mad_u32_u16 v42, v31, s34, v6 op_sel:[1,0,0,0]
	v_mad_u32_u16 v46, v32, s34, v6
	global_load_dwordx4 v[30:33], v39, s[20:21]
	s_nop 0
	global_load_dwordx4 v[34:37], v38, s[20:21]
	s_nop 0
	global_load_dwordx4 v[38:41], v40, s[20:21]
	s_nop 0
	global_load_dwordx4 v[42:45], v42, s[20:21]
	s_nop 0
	global_load_dwordx4 v[46:49], v46, s[20:21]
	s_nop 0
	s_waitcnt vmcnt(3)
	v_pk_add_f16 v33, v33, v37
	v_pk_add_f16 v32, v32, v36
	v_pk_add_f16 v31, v31, v35
	v_pk_add_f16 v30, v30, v34
	s_waitcnt vmcnt(1)
	v_pk_add_f16 v34, v41, v45
	v_pk_add_f16 v35, v40, v44
	v_pk_add_f16 v36, v39, v43
	v_pk_add_f16 v37, v38, v42
	v_pk_add_f16 v30, v30, v37
	v_pk_add_f16 v31, v31, v36
	v_pk_add_f16 v32, v32, v35
	v_pk_add_f16 v33, v33, v34
	s_waitcnt vmcnt(0)
	v_pk_add_f16 v30, v30, v46
	v_pk_add_f16 v31, v31, v47
	v_pk_add_f16 v32, v32, v48
	v_pk_add_f16 v33, v33, v49
	v_cvt_f32_f16_e32 v34, v30
	v_cvt_f32_f16_sdwa v35, v30 dst_sel:DWORD dst_unused:UNUSED_PAD src0_sel:WORD_1
	v_cvt_f32_f16_e32 v36, v31
	v_cvt_f32_f16_sdwa v37, v31 dst_sel:DWORD dst_unused:UNUSED_PAD src0_sel:WORD_1
	v_cvt_f32_f16_e32 v38, v32
	v_cvt_f32_f16_sdwa v39, v32 dst_sel:DWORD dst_unused:UNUSED_PAD src0_sel:WORD_1
	v_cvt_f32_f16_e32 v40, v33
	v_cvt_f32_f16_sdwa v41, v33 dst_sel:DWORD dst_unused:UNUSED_PAD src0_sel:WORD_1
	v_pk_add_f32 v[18:19], v[18:19], v[34:35]
	v_pk_add_f32 v[16:17], v[16:17], v[36:37]
	v_pk_add_f32 v[14:15], v[14:15], v[38:39]
	v_pk_add_f32 v[12:13], v[12:13], v[40:41]
	s_branch .Lagg_loop_done
.Lagg_n6:
	global_load_dwordx3 v[30:32], v[2:3], off
	s_waitcnt vmcnt(0)
	v_mad_u32_u16 v39, v30, s34, v6
	v_mad_u32_u16 v38, v30, s34, v6 op_sel:[1,0,0,0]
	v_mad_u32_u16 v40, v31, s34, v6
	v_mad_u32_u16 v42, v31, s34, v6 op_sel:[1,0,0,0]
	v_mad_u32_u16 v46, v32, s34, v6
	v_mad_u32_u16 v50, v32, s34, v6 op_sel:[1,0,0,0]
	global_load_dwordx4 v[30:33], v39, s[20:21]
	s_nop 0
	global_load_dwordx4 v[34:37], v38, s[20:21]
	s_nop 0
	global_load_dwordx4 v[38:41], v40, s[20:21]
	s_nop 0
	global_load_dwordx4 v[42:45], v42, s[20:21]
	s_nop 0
	global_load_dwordx4 v[46:49], v46, s[20:21]
	s_nop 0
	global_load_dwordx4 v[50:53], v50, s[20:21]
	s_nop 0
	s_waitcnt vmcnt(4)
	v_pk_add_f16 v33, v33, v37
	v_pk_add_f16 v32, v32, v36
	v_pk_add_f16 v31, v31, v35
	v_pk_add_f16 v30, v30, v34
	s_waitcnt vmcnt(2)
	v_pk_add_f16 v34, v41, v45
	v_pk_add_f16 v35, v40, v44
	v_pk_add_f16 v36, v39, v43
	v_pk_add_f16 v37, v38, v42
	v_pk_add_f16 v30, v30, v37
	v_pk_add_f16 v31, v31, v36
	v_pk_add_f16 v32, v32, v35
	v_pk_add_f16 v33, v33, v34
	s_waitcnt vmcnt(0)
	v_pk_add_f16 v38, v49, v53
	v_pk_add_f16 v39, v48, v52
	v_pk_add_f16 v40, v47, v51
	v_pk_add_f16 v41, v46, v50
	v_pk_add_f16 v30, v30, v41
	v_pk_add_f16 v31, v31, v40
	v_pk_add_f16 v32, v32, v39
	v_pk_add_f16 v33, v33, v38
	v_cvt_f32_f16_e32 v34, v30
	v_cvt_f32_f16_sdwa v35, v30 dst_sel:DWORD dst_unused:UNUSED_PAD src0_sel:WORD_1
	v_cvt_f32_f16_e32 v36, v31
	v_cvt_f32_f16_sdwa v37, v31 dst_sel:DWORD dst_unused:UNUSED_PAD src0_sel:WORD_1
	v_cvt_f32_f16_e32 v38, v32
	v_cvt_f32_f16_sdwa v39, v32 dst_sel:DWORD dst_unused:UNUSED_PAD src0_sel:WORD_1
	v_cvt_f32_f16_e32 v40, v33
	v_cvt_f32_f16_sdwa v41, v33 dst_sel:DWORD dst_unused:UNUSED_PAD src0_sel:WORD_1
	v_pk_add_f32 v[18:19], v[18:19], v[34:35]
	v_pk_add_f32 v[16:17], v[16:17], v[36:37]
	v_pk_add_f32 v[14:15], v[14:15], v[38:39]
	v_pk_add_f32 v[12:13], v[12:13], v[40:41]
	s_branch .Lagg_loop_done
.Lagg_n7:
	global_load_dwordx4 v[30:33], v[2:3], off
	s_waitcnt vmcnt(0)
	v_mad_u32_u16 v39, v30, s34, v6
	v_mad_u32_u16 v38, v30, s34, v6 op_sel:[1,0,0,0]
	v_mad_u32_u16 v40, v31, s34, v6
	v_mad_u32_u16 v42, v31, s34, v6 op_sel:[1,0,0,0]
	v_mad_u32_u16 v46, v32, s34, v6
	v_mad_u32_u16 v50, v32, s34, v6 op_sel:[1,0,0,0]
	v_mad_u32_u16 v54, v33, s34, v6
	global_load_dwordx4 v[30:33], v39, s[20:21]
	s_nop 0
	global_load_dwordx4 v[34:37], v38, s[20:21]
	s_nop 0
	global_load_dwordx4 v[38:41], v40, s[20:21]
	s_nop 0
	global_load_dwordx4 v[42:45], v42, s[20:21]
	s_nop 0
	global_load_dwordx4 v[46:49], v46, s[20:21]
	s_nop 0
	global_load_dwordx4 v[50:53], v50, s[20:21]
	s_nop 0
	global_load_dwordx4 v[54:57], v54, s[20:21]
	s_nop 0
	s_waitcnt vmcnt(5)
	v_pk_add_f16 v33, v33, v37
	v_pk_add_f16 v32, v32, v36
	v_pk_add_f16 v31, v31, v35
	v_pk_add_f16 v30, v30, v34
	s_waitcnt vmcnt(3)
	v_pk_add_f16 v34, v41, v45
	v_pk_add_f16 v35, v40, v44
	v_pk_add_f16 v36, v39, v43
	v_pk_add_f16 v37, v38, v42
	v_pk_add_f16 v30, v30, v37
	v_pk_add_f16 v31, v31, v36
	v_pk_add_f16 v32, v32, v35
	v_pk_add_f16 v33, v33, v34
	s_waitcnt vmcnt(1)
	v_pk_add_f16 v38, v49, v53
	v_pk_add_f16 v39, v48, v52
	v_pk_add_f16 v40, v47, v51
	v_pk_add_f16 v41, v46, v50
	s_waitcnt vmcnt(0)
	v_pk_add_f16 v41, v41, v54
	v_pk_add_f16 v40, v40, v55
	v_pk_add_f16 v39, v39, v56
	v_pk_add_f16 v38, v38, v57
	v_pk_add_f16 v30, v30, v41
	v_pk_add_f16 v31, v31, v40
	v_pk_add_f16 v32, v32, v39
	v_pk_add_f16 v33, v33, v38
	v_cvt_f32_f16_e32 v34, v30
	v_cvt_f32_f16_sdwa v35, v30 dst_sel:DWORD dst_unused:UNUSED_PAD src0_sel:WORD_1
	v_cvt_f32_f16_e32 v36, v31
	v_cvt_f32_f16_sdwa v37, v31 dst_sel:DWORD dst_unused:UNUSED_PAD src0_sel:WORD_1
	v_cvt_f32_f16_e32 v38, v32
	v_cvt_f32_f16_sdwa v39, v32 dst_sel:DWORD dst_unused:UNUSED_PAD src0_sel:WORD_1
	v_cvt_f32_f16_e32 v40, v33
	v_cvt_f32_f16_sdwa v41, v33 dst_sel:DWORD dst_unused:UNUSED_PAD src0_sel:WORD_1
	v_pk_add_f32 v[18:19], v[18:19], v[34:35]
	v_pk_add_f32 v[16:17], v[16:17], v[36:37]
	v_pk_add_f32 v[14:15], v[14:15], v[38:39]
	v_pk_add_f32 v[12:13], v[12:13], v[40:41]
	s_branch .Lagg_loop_done

	.amdhsa_kernel _Z6k_agg1PKDF16_PK15HIP_vector_typeIiLj2EEPKtPKfS8_S8_Pf
		.amdhsa_group_segment_fixed_size 2304
		.amdhsa_private_segment_fixed_size 0
		.amdhsa_kernarg_size 56
		.amdhsa_user_sgpr_count 2
		.amdhsa_user_sgpr_dispatch_ptr 0
		.amdhsa_user_sgpr_queue_ptr 0
		.amdhsa_user_sgpr_kernarg_segment_ptr 1
		.amdhsa_user_sgpr_dispatch_id 0
		.amdhsa_user_sgpr_kernarg_preload_length 0
		.amdhsa_user_sgpr_kernarg_preload_offset 0
		.amdhsa_user_sgpr_private_segment_size 0
		.amdhsa_uses_dynamic_stack 0
		.amdhsa_enable_private_segment 0
		.amdhsa_system_sgpr_workgroup_id_x 1
		.amdhsa_system_sgpr_workgroup_id_y 0
		.amdhsa_system_sgpr_workgroup_id_z 0
		.amdhsa_system_sgpr_workgroup_info 0
		.amdhsa_system_vgpr_workitem_id 0
		.amdhsa_next_free_vgpr 63
		.amdhsa_next_free_sgpr 35
		.amdhsa_accum_offset 64
		.amdhsa_reserve_vcc 1
		.amdhsa_float_round_mode_32 0
		.amdhsa_float_round_mode_16_64 0
		.amdhsa_float_denorm_mode_32 3
		.amdhsa_float_denorm_mode_16_64 3
		.amdhsa_dx10_clamp 1
		.amdhsa_ieee_mode 1
		.amdhsa_fp16_overflow 0
		.amdhsa_tg_split 0
		.amdhsa_exception_fp_ieee_invalid_op 0
		.amdhsa_exception_fp_denorm_src 0
		.amdhsa_exception_fp_ieee_div_zero 0
		.amdhsa_exception_fp_ieee_overflow 0
		.amdhsa_exception_fp_ieee_underflow 0
		.amdhsa_exception_fp_ieee_inexact 0
		.amdhsa_exception_int_div_zero 0
	.end_amdhsa_kernel

amdhsa.kernels:
  - .agpr_count:     0
    .args:
      - .actual_access:  read_only
        .address_space:  global
        .offset:         0
        .size:           8
        .value_kind:     global_buffer
      - .actual_access:  write_only
        .address_space:  global
        .offset:         8
        .size:           8
        .value_kind:     global_buffer
      - .actual_access:  write_only
        .address_space:  global
        .offset:         16
        .size:           8
        .value_kind:     global_buffer
      - .actual_access:  read_only
        .address_space:  global
        .offset:         24
        .size:           8
        .value_kind:     global_buffer
      - .actual_access:  write_only
        .address_space:  global
        .offset:         32
        .size:           8
        .value_kind:     global_buffer
      - .actual_access:  write_only
        .address_space:  global
        .offset:         40
        .size:           8
        .value_kind:     global_buffer
    .group_segment_fixed_size: 14576
    .kernarg_segment_align: 8
    .kernarg_segment_size: 48
    .language:       OpenCL C
    .language_version:
      - 2
      - 0
    .max_flat_workgroup_size: 256
    .name:           _Z5k_binPKiPiPjPKfPDv8_DF16_PDF16_
    .private_segment_fixed_size: 0
    .sgpr_count:     22
    .sgpr_spill_count: 0
    .symbol:         _Z5k_binPKiPiPjPKfPDv8_DF16_PDF16_.kd
    .uniform_work_group_size: 1
    .uses_dynamic_stack: false
    .vgpr_count:     75
    .vgpr_spill_count: 0
    .wavefront_size: 64
  - .agpr_count:     0
    .args:
      - .actual_access:  read_only
        .address_space:  global
        .offset:         0
        .size:           8
        .value_kind:     global_buffer
      - .actual_access:  read_only
        .address_space:  global
        .offset:         8
        .size:           8
        .value_kind:     global_buffer
      - .actual_access:  write_only
        .address_space:  global
        .offset:         16
        .size:           8
        .value_kind:     global_buffer
      - .actual_access:  write_only
        .address_space:  global
        .offset:         24
        .size:           8
        .value_kind:     global_buffer
      - .actual_access:  write_only
        .address_space:  global
        .offset:         32
        .size:           8
        .value_kind:     global_buffer
      - .actual_access:  write_only
        .address_space:  global
        .offset:         40
        .size:           8
        .value_kind:     global_buffer
    .group_segment_fixed_size: 18452
    .kernarg_segment_align: 8
    .kernarg_segment_size: 48
    .language:       OpenCL C
    .language_version:
      - 2
      - 0
    .max_flat_workgroup_size: 256
    .name:           _Z5k_csrPKiPKjP15HIP_vector_typeIiLj2EEPfPtS6_
    .private_segment_fixed_size: 0
    .sgpr_count:     94
    .sgpr_spill_count: 0
    .symbol:         _Z5k_csrPKiPKjP15HIP_vector_typeIiLj2EEPfPtS6_.kd
    .uniform_work_group_size: 1
    .uses_dynamic_stack: false
    .vgpr_count:     65
    .vgpr_spill_count: 0
    .wavefront_size: 64
  - .agpr_count:     0
    .args:
      - .actual_access:  read_only
        .address_space:  global
        .offset:         0
        .size:           8
        .value_kind:     global_buffer
      - .actual_access:  read_only
        .address_space:  global
        .offset:         8
        .size:           8
        .value_kind:     global_buffer
      - .actual_access:  read_only
        .address_space:  global
        .offset:         16
        .size:           8
        .value_kind:     global_buffer
      - .actual_access:  read_only
        .address_space:  global
        .offset:         24
        .size:           8
        .value_kind:     global_buffer
      - .actual_access:  write_only
        .address_space:  global
        .offset:         32
        .size:           8
        .value_kind:     global_buffer
    .group_segment_fixed_size: 129152
    .kernarg_segment_align: 8
    .kernarg_segment_size: 40
    .language:       OpenCL C
    .language_version:
      - 2
      - 0
    .max_flat_workgroup_size: 512
    .name:           _Z6k_gemmPKfPKDv8_DF16_S0_S0_PDF16_
    .private_segment_fixed_size: 0
    .sgpr_count:     22
    .sgpr_spill_count: 0
    .symbol:         _Z6k_gemmPKfPKDv8_DF16_S0_S0_PDF16_.kd
    .uniform_work_group_size: 1
    .uses_dynamic_stack: false
    .vgpr_count:     256
    .vgpr_spill_count: 0
    .wavefront_size: 64
  - .agpr_count:     0
    .args:
      - .actual_access:  read_only
        .address_space:  global
        .offset:         0
        .size:           8
        .value_kind:     global_buffer
      - .actual_access:  read_only
        .address_space:  global
        .offset:         8
        .size:           8
        .value_kind:     global_buffer
      - .actual_access:  read_only
        .address_space:  global
        .offset:         16
        .size:           8
        .value_kind:     global_buffer
      - .actual_access:  read_only
        .address_space:  global
        .offset:         24
        .size:           8
        .value_kind:     global_buffer
      - .actual_access:  read_only
        .address_space:  global
        .offset:         32
        .size:           8
        .value_kind:     global_buffer
      - .actual_access:  read_only
        .address_space:  global
        .offset:         40
        .size:           8
        .value_kind:     global_buffer
      - .address_space:  global
        .offset:         48
        .size:           8
        .value_kind:     global_buffer
    .group_segment_fixed_size: 2304
    .kernarg_segment_align: 8
    .kernarg_segment_size: 56
    .language:       OpenCL C
    .language_version:
      - 2
      - 0
    .max_flat_workgroup_size: 320
    .name:           _Z6k_agg1PKDF16_PK15HIP_vector_typeIiLj2EEPKtPKfS8_S8_Pf
    .private_segment_fixed_size: 0
    .sgpr_count:     41
    .sgpr_spill_count: 0
    .symbol:         _Z6k_agg1PKDF16_PK15HIP_vector_typeIiLj2EEPKtPKfS8_S8_Pf.kd
    .uniform_work_group_size: 1
    .uses_dynamic_stack: false
    .vgpr_count:     63
    .vgpr_spill_count: 0
    .wavefront_size: 64
  - .agpr_count:     0
    .args:
      - .actual_access:  read_only
        .address_space:  global
        .offset:         0
        .size:           8
        .value_kind:     global_buffer
      - .actual_access:  read_only
        .address_space:  global
        .offset:         8
        .size:           8
        .value_kind:     global_buffer
      - .actual_access:  read_only
        .address_space:  global
        .offset:         16
        .size:           8
        .value_kind:     global_buffer
      - .actual_access:  read_only
        .address_space:  global
        .offset:         24
        .size:           8
        .value_kind:     global_buffer
      - .actual_access:  read_only
        .address_space:  global
        .offset:         32
        .size:           8
        .value_kind:     global_buffer
      - .actual_access:  write_only
        .address_space:  global
        .offset:         40
        .size:           8
        .value_kind:     global_buffer
    .group_segment_fixed_size: 0
    .kernarg_segment_align: 8
    .kernarg_segment_size: 48
    .language:       OpenCL C
    .language_version:
      - 2
      - 0
    .max_flat_workgroup_size: 256
    .name:           _Z5k_outPKfPK15HIP_vector_typeIiLj2EEPKtS0_S0_Pf
    .private_segment_fixed_size: 0
    .sgpr_count:     18
    .sgpr_spill_count: 0
    .symbol:         _Z5k_outPKfPK15HIP_vector_typeIiLj2EEPKtS0_S0_Pf.kd
    .uniform_work_group_size: 1
    .uses_dynamic_stack: false
    .vgpr_count:     27
    .vgpr_spill_count: 0
    .wavefront_size: 64
